# v19_bperm
# speedup vs baseline: 1.0028x; 1.0028x over previous
.LBB1_113:
	s_or_b64 exec, exec, s[54:55]
	s_waitcnt lgkmcnt(2)
	v_rsq_f32_e32 v167, v166
	v_mul_f32_e32 v166, 0.5, v166
	s_lshl_b32 s54, s96, 2
	v_add3_u32 v165, v128, s54, v165
	s_waitcnt lgkmcnt(1)
	v_mul_f32_e32 v168, v166, v167
	v_fma_f32 v168, -v167, v168, s58
	v_mul_f32_e32 v167, v167, v168
	v_mul_f32_e32 v166, v166, v167
	v_fma_f32 v166, -v167, v166, s58
	v_mul_f32_e32 v167, v167, v166
	ds_bpermute_b32 v169, v129, v167
	ds_bpermute_b32 v168, v142, v167
	ds_bpermute_b32 v166, v143, v167
	ds_bpermute_b32 v167, v144, v167
	s_add_i32 s54, s54, 0x1dc00
	s_waitcnt lgkmcnt(3)
	v_mul_f32_e32 v66, v66, v169
	v_mul_f32_e32 v70, v70, v169
	s_waitcnt lgkmcnt(2)
	v_mul_f32_e32 v71, v71, v168
	v_cndmask_b32_e64 v70, v70, 0, s[40:41]
	v_cndmask_b32_e64 v71, v71, 0, s[42:43]
	ds_write2_b32 v165, v70, v71 offset1:68
	s_waitcnt lgkmcnt(2)
	v_mul_f32_e32 v70, v72, v166
	s_waitcnt lgkmcnt(1)
	v_mul_f32_e32 v71, v73, v167
	v_cndmask_b32_e64 v70, v70, 0, s[44:45]
	v_cndmask_b32_e64 v71, v71, 0, s[50:51]
	v_mul_f32_e32 v67, v67, v168
	v_pk_mul_f32 v[68:69], v[68:69], v[166:167]
	ds_write2_b32 v165, v70, v71 offset0:136 offset1:204
	v_mul_u32_u24_e32 v70, s95, v164
	v_cndmask_b32_e64 v66, v66, 0, s[38:39]
	v_cndmask_b32_e64 v67, 0, v67, s[40:41]
	v_cndmask_b32_e64 v69, v69, 0, s[46:47]
	v_cndmask_b32_e64 v68, v68, 0, s[48:49]
	v_add3_u32 v70, s54, v70, v148
	ds_write_b128 v70, v[66:69]

.LBB1_133:
	v_or_b32_e32 v50, s94, v133
	s_movk_i32 s54, 0x110
	v_lshlrev_b32_e32 v6, 5, v132
	s_lshl_b32 s94, s87, 5
	v_mad_u32_u24 v58, v50, s54, v6
	v_or_b32_e32 v2, s94, v133
	s_movk_i32 s54, 0x44
	s_waitcnt lgkmcnt(0)
	s_barrier
	v_mul_u32_u24_e32 v60, s54, v2
	ds_read_b128 v[2:5], v58
	ds_read_b128 v[8:11], v58 offset:16
	s_mov_b32 s54, 0x42800000
	v_lshl_add_u32 v6, v60, 2, v6
	ds_read_b128 v[12:15], v6 offset:17408
	ds_read_b128 v[16:19], v6 offset:17424
	s_waitcnt lgkmcnt(3)
	v_fma_mixlo_f16 v7, v2, s54, 0
	v_mov_b32_e32 v2, v3
	v_mov_b32_e32 v3, v4
	v_pk_mul_f32 v[2:3], v[2:3], s[54:55] op_sel_hi:[1,0]
	s_waitcnt lgkmcnt(2)
	v_pk_mov_b32 v[4:5], v[4:5], v[8:9] op_sel:[1,0]
	v_cvt_pk_f16_f32 v3, v2, v3
	v_pk_mul_f32 v[4:5], v[4:5], s[54:55] op_sel_hi:[1,0]
	v_pack_b32_f16 v2, v7, v3
	v_cvt_pk_f16_f32 v7, v4, v5
	v_mov_b32_e32 v4, v9
	v_mov_b32_e32 v5, v10
	v_pk_mul_f32 v[4:5], v[4:5], s[54:55] op_sel_hi:[1,0]
	s_waitcnt lgkmcnt(0)
	v_cvt_pk_f16_f32 v10, v16, v17
	v_cvt_pk_f16_f32 v5, v4, v5
	v_alignbit_b32 v4, v5, v7, 16
	v_lshrrev_b32_e32 v5, 16, v5
	v_fma_mixhi_f16 v5, v11, s54, 0
	v_cvt_pk_f16_f32 v11, v18, v19
	v_cvt_pk_f16_f32 v9, v14, v15
	v_cvt_pk_f16_f32 v8, v12, v13
	v_alignbit_b32 v3, v7, v3, 16
	v_lshlrev_b32_e32 v62, 3, v132
	v_add_u32_e32 v56, 0x8800, v6
	v_mfma_f32_32x32x16_f16 a[16:31], v[8:11], v[2:5], 0
	v_accvgpr_write_b32 a0, 0
	ds_read_b128 v[8:11], v56 offset:16
	ds_read_b128 v[12:15], v56
	s_waitcnt lgkmcnt(1)
	v_cvt_pk_f16_f32 v11, v10, v11
	v_cvt_pk_f16_f32 v10, v8, v9
	s_waitcnt lgkmcnt(0)
	v_cvt_pk_f16_f32 v9, v14, v15
	v_cvt_pk_f16_f32 v8, v12, v13
	s_nop 1
	v_mfma_f32_32x32x16_f16 a[0:15], v[8:11], v[2:5], 0
	s_branch .LBB1_136
	v_accvgpr_mov_b32 a1, a0
	v_accvgpr_mov_b32 a2, a0
	v_accvgpr_mov_b32 a3, a0
	v_accvgpr_mov_b32 a4, a0
	v_accvgpr_mov_b32 a5, a0
	v_accvgpr_mov_b32 a6, a0
	v_accvgpr_mov_b32 a7, a0
	v_accvgpr_mov_b32 a8, a0
	v_accvgpr_mov_b32 a9, a0
	v_accvgpr_mov_b32 a10, a0
	v_accvgpr_mov_b32 a11, a0
	v_accvgpr_mov_b32 a12, a0
	v_accvgpr_mov_b32 a13, a0
	v_accvgpr_mov_b32 a14, a0
	v_accvgpr_mov_b32 a15, a0

.LBB1_234:
	s_or_b64 exec, exec, s[52:53]
	s_waitcnt lgkmcnt(2)
	v_rsq_f32_e32 v17, v16
	v_mul_f32_e32 v16, 0.5, v16
	s_lshl_b32 s52, s97, 2
	v_add3_u32 v15, v128, s52, v15
	s_waitcnt lgkmcnt(1)
	v_mul_f32_e32 v18, v16, v17
	v_fma_f32 v18, -v17, v18, s58
	v_mul_f32_e32 v17, v17, v18
	v_mul_f32_e32 v16, v16, v17
	v_fma_f32 v16, -v17, v16, s58
	v_mul_f32_e32 v17, v17, v16
	ds_bpermute_b32 v19, v129, v17
	ds_bpermute_b32 v18, v142, v17
	ds_bpermute_b32 v16, v143, v17
	ds_bpermute_b32 v17, v144, v17
	s_add_i32 s52, s52, 0x19800
	s_waitcnt lgkmcnt(3)
	v_mul_f32_e32 v2, v2, v19
	v_mul_f32_e32 v6, v6, v19
	s_waitcnt lgkmcnt(2)
	v_mul_f32_e32 v7, v7, v18
	v_cndmask_b32_e64 v6, v6, 0, s[40:41]
	v_cndmask_b32_e64 v7, v7, 0, s[42:43]
	ds_write2_b32 v15, v6, v7 offset1:68
	s_waitcnt lgkmcnt(2)
	v_mul_f32_e32 v6, v8, v16
	s_waitcnt lgkmcnt(1)
	v_mul_f32_e32 v7, v9, v17
	v_cndmask_b32_e64 v6, v6, 0, s[44:45]
	v_cndmask_b32_e64 v7, v7, 0, s[50:51]
	v_mul_f32_e32 v3, v3, v18
	v_pk_mul_f32 v[4:5], v[4:5], v[16:17]
	ds_write2_b32 v15, v6, v7 offset0:136 offset1:204
	v_mul_u32_u24_e32 v6, s57, v14
	v_cndmask_b32_e64 v2, v2, 0, s[38:39]
	v_cndmask_b32_e64 v3, 0, v3, s[40:41]
	v_cndmask_b32_e64 v5, v5, 0, s[46:47]
	v_cndmask_b32_e64 v4, v4, 0, s[48:49]
	v_add3_u32 v6, s52, v6, v148
	ds_write_b128 v6, v[2:5]

.LBB1_328:
	s_waitcnt lgkmcnt(0)
	v_lshl_or_b32 v3, s88, 5, v133
	v_lshlrev_b32_e32 v0, 5, v132
	s_movk_i32 s64, 0x110
	v_mad_u32_u24 v2, v3, s64, v0
	s_lshl_b32 s53, s87, 5
	ds_read_b128 v[4:7], v2
	ds_read_b128 v[54:57], v2 offset:16
	v_or_b32_e32 v1, s53, v133
	v_mad_u64_u32 v[0:1], s[54:55], v1, s64, v[0:1]
	ds_read_b128 v[58:61], v0 offset:17408
	ds_read_b128 v[62:65], v0 offset:17424
	s_mov_b32 s54, 0x42800000
	s_waitcnt lgkmcnt(3)
	v_fma_mixlo_f16 v1, v4, s54, 0
	v_mov_b32_e32 v4, v5
	v_mov_b32_e32 v5, v6
	v_pk_mul_f32 v[4:5], v[4:5], s[54:55] op_sel_hi:[1,0]
	s_waitcnt lgkmcnt(2)
	v_pk_mov_b32 v[6:7], v[6:7], v[54:55] op_sel:[1,0]
	v_cvt_pk_f16_f32 v5, v4, v5
	v_pk_mul_f32 v[6:7], v[6:7], s[54:55] op_sel_hi:[1,0]
	v_pack_b32_f16 v4, v1, v5
	v_cvt_pk_f16_f32 v1, v6, v7
	v_mov_b32_e32 v6, v55
	v_mov_b32_e32 v7, v56
	s_waitcnt lgkmcnt(0)
	v_cvt_pk_f16_f32 v65, v64, v65
	v_cvt_pk_f16_f32 v64, v62, v63
	v_cvt_pk_f16_f32 v63, v60, v61
	v_cvt_pk_f16_f32 v62, v58, v59
	v_pk_mul_f32 v[6:7], v[6:7], s[54:55] op_sel_hi:[1,0]
	ds_read_b128 v[58:61], v2 offset:64
	v_cvt_pk_f16_f32 v7, v6, v7
	v_alignbit_b32 v6, v7, v1, 16
	v_lshrrev_b32_e32 v7, 16, v7
	v_alignbit_b32 v5, v1, v5, 16
	v_fma_mixhi_f16 v7, v57, s54, 0
	s_mov_b32 s52, 0
	s_mov_b32 s65, 2
	v_mfma_f32_32x32x16_f16 a[0:15], v[62:65], v[4:7], 0
	ds_read_b128 v[4:7], v2 offset:80
	s_waitcnt lgkmcnt(1)
	v_mov_b32_e32 v8, v59
	v_mov_b32_e32 v9, v60
	v_mul_f32_e64 v8, v8, s54
	v_mul_f32_e64 v9, v9, s54
	v_fma_mixlo_f16 v1, v58, s54, 0
	v_cvt_pk_f16_f32 v53, v8, v9
	s_waitcnt lgkmcnt(0)
	v_pk_mov_b32 v[8:9], v[60:61], v[4:5] op_sel:[1,0]
	ds_read_b128 v[56:59], v0 offset:17472
	ds_read_b128 v[60:63], v0 offset:17488
	v_mov_b32_e32 v4, v5
	v_mov_b32_e32 v5, v6
	v_pk_mul_f32 v[4:5], v[4:5], s[54:55] op_sel_hi:[1,0]
	v_pk_mul_f32 v[8:9], v[8:9], s[54:55] op_sel_hi:[1,0]
	s_waitcnt lgkmcnt(0)
	v_cvt_pk_f16_f32 v63, v62, v63
	v_cvt_pk_f16_f32 v62, v60, v61
	v_cvt_pk_f16_f32 v61, v58, v59
	v_cvt_pk_f16_f32 v60, v56, v57
	v_cvt_pk_f16_f32 v4, v4, v5
	v_pack_b32_f16 v54, v1, v53
	v_cvt_pk_f16_f32 v1, v8, v9
	ds_read_b128 v[64:67], v2 offset:128
	v_lshrrev_b32_e32 v57, 16, v4
	v_alignbit_b32 v55, v1, v53, 16
	v_alignbit_b32 v56, v4, v1, 16
	v_fma_mixhi_f16 v57, v7, s54, 0
	ds_read_b128 v[4:7], v2 offset:144
	s_waitcnt lgkmcnt(1)
	v_mov_b32_e32 v8, v65
	v_mfma_f32_32x32x16_f16 a[0:15], v[60:63], v[54:57], a[0:15]
	ds_read_b128 v[56:59], v0 offset:17536
	ds_read_b128 v[60:63], v0 offset:17552
	v_mov_b32_e32 v9, v66
	v_mul_f32_e64 v8, v8, s54
	v_mul_f32_e64 v9, v9, s54
	v_fma_mixlo_f16 v1, v64, s54, 0
	v_cvt_pk_f16_f32 v53, v8, v9
	s_waitcnt lgkmcnt(2)
	v_pk_mov_b32 v[8:9], v[66:67], v[4:5] op_sel:[1,0]
	v_mov_b32_e32 v4, v5
	v_mov_b32_e32 v5, v6
	s_waitcnt lgkmcnt(0)
	v_cvt_pk_f16_f32 v63, v62, v63
	v_cvt_pk_f16_f32 v62, v60, v61
	v_cvt_pk_f16_f32 v61, v58, v59
	v_cvt_pk_f16_f32 v60, v56, v57
	v_pk_mul_f32 v[4:5], v[4:5], s[54:55] op_sel_hi:[1,0]
	v_pk_mul_f32 v[8:9], v[8:9], s[54:55] op_sel_hi:[1,0]
	v_cvt_pk_f16_f32 v4, v4, v5
	v_pack_b32_f16 v54, v1, v53
	v_cvt_pk_f16_f32 v1, v8, v9
	ds_read_b128 v[64:67], v2 offset:192
	v_lshrrev_b32_e32 v57, 16, v4
	v_alignbit_b32 v55, v1, v53, 16
	v_alignbit_b32 v56, v4, v1, 16
	v_fma_mixhi_f16 v57, v7, s54, 0
	ds_read_b128 v[4:7], v2 offset:208
	s_waitcnt lgkmcnt(1)
	v_mov_b32_e32 v8, v65
	v_mfma_f32_32x32x16_f16 a[0:15], v[60:63], v[54:57], a[0:15]
	ds_read_b128 v[56:59], v0 offset:17600
	ds_read_b128 v[60:63], v0 offset:17616
	v_mov_b32_e32 v9, v66
	v_mul_f32_e64 v8, v8, s54
	v_mul_f32_e64 v9, v9, s54
	v_fma_mixlo_f16 v1, v64, s54, 0
	v_cvt_pk_f16_f32 v53, v8, v9
	s_waitcnt lgkmcnt(2)
	v_pk_mov_b32 v[8:9], v[66:67], v[4:5] op_sel:[1,0]
	v_mov_b32_e32 v4, v5
	v_mov_b32_e32 v5, v6
	s_waitcnt lgkmcnt(0)
	v_cvt_pk_f16_f32 v63, v62, v63
	v_cvt_pk_f16_f32 v62, v60, v61
	v_cvt_pk_f16_f32 v61, v58, v59
	v_cvt_pk_f16_f32 v60, v56, v57
	v_pk_mul_f32 v[4:5], v[4:5], s[54:55] op_sel_hi:[1,0]
	v_pk_mul_f32 v[8:9], v[8:9], s[54:55] op_sel_hi:[1,0]
	v_cvt_pk_f16_f32 v4, v4, v5
	v_pack_b32_f16 v54, v1, v53
	v_cvt_pk_f16_f32 v1, v8, v9
	v_lshrrev_b32_e32 v57, 16, v4
	v_alignbit_b32 v55, v1, v53, 16
	v_alignbit_b32 v56, v4, v1, 16
	v_fma_mixhi_f16 v57, v7, s54, 0
	v_lshl_or_b32 v1, v132, 2, s53
	s_movk_i32 s53, 0x44
	v_mfma_f32_32x32x16_f16 a[0:15], v[60:63], v[54:57], a[0:15]
	v_mul_u32_u24_e32 v1, s53, v1
	v_add_lshl_u32 v60, v3, v1, 2
	v_add_u32_e32 v3, 0x4400, v60
	s_barrier
	s_add_u32 s53, s66, s74
	s_addc_u32 s55, s67, s75
	s_add_u32 s72, s53, s72
	s_addc_u32 s73, s55, s73
	v_lshlrev_b32_e32 v8, 2, v14
	v_mov_b32_e32 v9, 0
	s_nop 1
	v_accvgpr_read_b32 v4, a0
	v_accvgpr_read_b32 v1, a1
	v_mul_f32_e32 v4, 0x3c800000, v4
	v_mul_f32_e32 v1, 0x3c800000, v1
	ds_write2_b32 v3, v4, v1 offset1:68
	v_accvgpr_read_b32 v1, a2
	v_accvgpr_read_b32 v4, a3
	v_mul_f32_e32 v1, 0x3c800000, v1
	v_mul_f32_e32 v4, 0x3c800000, v4
	ds_write2_b32 v3, v1, v4 offset0:136 offset1:204
	v_accvgpr_read_b32 v1, a4
	v_accvgpr_read_b32 v3, a5
	v_mul_f32_e32 v1, 0x3c800000, v1
	v_mul_f32_e32 v3, 0x3c800000, v3
	v_add_u32_e32 v4, 0x4c00, v60
	ds_write2_b32 v4, v1, v3 offset0:32 offset1:100
	v_accvgpr_read_b32 v1, a6
	v_accvgpr_read_b32 v3, a7
	v_mul_f32_e32 v1, 0x3c800000, v1
	v_mul_f32_e32 v3, 0x3c800000, v3
	ds_write2_b32 v4, v1, v3 offset0:168 offset1:236
	v_accvgpr_read_b32 v1, a8
	v_accvgpr_read_b32 v3, a9
	v_mul_f32_e32 v1, 0x3c800000, v1
	v_mul_f32_e32 v3, 0x3c800000, v3
	v_add_u32_e32 v4, 0x5400, v60
	ds_write2_b32 v4, v1, v3 offset0:64 offset1:132
	v_accvgpr_read_b32 v1, a10
	v_accvgpr_read_b32 v3, a11
	v_mul_f32_e32 v1, 0x3c800000, v1
	v_mul_f32_e32 v3, 0x3c800000, v3
	v_add_u32_e32 v4, 0x5600, v60
	ds_write2_b32 v4, v1, v3 offset0:72 offset1:140
	v_accvgpr_read_b32 v1, a12
	v_accvgpr_read_b32 v3, a13
	v_mul_f32_e32 v1, 0x3c800000, v1
	v_mul_f32_e32 v3, 0x3c800000, v3
	v_add_u32_e32 v4, 0x5c00, v60
	ds_write2_b32 v4, v1, v3 offset0:96 offset1:164
	v_accvgpr_read_b32 v1, a14
	v_accvgpr_read_b32 v3, a15
	v_mul_f32_e32 v1, 0x3c800000, v1
	v_mul_f32_e32 v3, 0x3c800000, v3
	v_add_u32_e32 v4, 0x5e00, v60
	ds_write2_b32 v4, v1, v3 offset0:104 offset1:172
	s_waitcnt lgkmcnt(0)
	s_barrier
	ds_read_b128 v[4:7], v52
	v_lshl_add_u64 v[56:57], s[72:73], 0, v[8:9]
	v_lshlrev_b32_e32 v8, 9, v46
	v_lshl_add_u64 v[58:59], v[8:9], 2, v[56:57]
	ds_read_b128 v[52:55], v51
	s_waitcnt lgkmcnt(1)
	global_store_dwordx4 v[58:59], v[4:7], off
	v_lshlrev_b32_e32 v8, 9, v48
	ds_read_b128 v[4:7], v50
	v_lshl_add_u64 v[58:59], v[8:9], 2, v[56:57]
	v_lshlrev_b32_e32 v8, 9, v47
	ds_read_b128 v[46:49], v49
	v_lshl_add_u64 v[50:51], v[8:9], 2, v[56:57]
	v_lshlrev_b32_e32 v8, 9, v45
	s_waitcnt lgkmcnt(2)
	global_store_dwordx4 v[58:59], v[52:55], off
	s_waitcnt lgkmcnt(1)
	global_store_dwordx4 v[50:51], v[4:7], off
	ds_read_b128 v[4:7], v0 offset:17408
	v_lshl_add_u64 v[50:51], v[8:9], 2, v[56:57]
	s_waitcnt lgkmcnt(1)
	global_store_dwordx4 v[50:51], v[46:49], off
	ds_read_b128 v[46:49], v0 offset:17424
	ds_read_b128 v[50:53], v2 offset:17408
	s_waitcnt lgkmcnt(2)
	v_fma_mixlo_f16 v1, v4, s54, 0
	v_mov_b32_e32 v4, v5
	v_mov_b32_e32 v5, v6
	v_pk_mul_f32 v[4:5], v[4:5], s[54:55] op_sel_hi:[1,0]
	s_waitcnt lgkmcnt(1)
	v_pk_mov_b32 v[6:7], v[6:7], v[46:47] op_sel:[1,0]
	v_cvt_pk_f16_f32 v3, v4, v5
	v_pk_mul_f32 v[6:7], v[6:7], s[54:55] op_sel_hi:[1,0]
	v_pack_b32_f16 v4, v1, v3
	v_cvt_pk_f16_f32 v1, v6, v7
	v_mov_b32_e32 v6, v47
	v_mov_b32_e32 v7, v48
	v_pk_mul_f32 v[6:7], v[6:7], s[54:55] op_sel_hi:[1,0]
	v_alignbit_b32 v5, v1, v3, 16
	v_cvt_pk_f16_f32 v3, v6, v7
	v_lshrrev_b32_e32 v7, 16, v3
	v_fma_mixhi_f16 v7, v49, s54, 0
	ds_read_b128 v[46:49], v2 offset:17424
	v_alignbit_b32 v6, v3, v1, 16
	s_waitcnt lgkmcnt(1)
	v_fma_mixlo_f16 v1, v50, s54, 0
	v_mov_b32_e32 v50, v51
	v_mov_b32_e32 v51, v52
	v_pk_mul_f32 v[50:51], v[50:51], s[54:55] op_sel_hi:[1,0]
	s_waitcnt lgkmcnt(0)
	v_pk_mov_b32 v[52:53], v[52:53], v[46:47] op_sel:[1,0]
	v_cvt_pk_f16_f32 v3, v50, v51
	v_pk_mul_f32 v[52:53], v[52:53], s[54:55] op_sel_hi:[1,0]
	v_mov_b32_e32 v46, v47
	v_mov_b32_e32 v47, v48
	v_pack_b32_f16 v50, v1, v3
	v_cvt_pk_f16_f32 v1, v52, v53
	v_pk_mul_f32 v[46:47], v[46:47], s[54:55] op_sel_hi:[1,0]
	v_alignbit_b32 v51, v1, v3, 16
	v_cvt_pk_f16_f32 v3, v46, v47
	v_lshrrev_b32_e32 v53, 16, v3
	v_alignbit_b32 v52, v3, v1, 16
	ds_read_b128 v[54:57], v0 offset:17472
	v_fma_mixhi_f16 v53, v49, s54, 0
	s_mov_b32 s53, s52
	s_mov_b32 s72, 0x19800
	v_mfma_f32_32x32x16_f16 a[0:15], v[4:7], v[50:53], 0
	ds_read_b128 v[4:7], v0 offset:17488
	s_waitcnt lgkmcnt(1)
	v_mov_b32_e32 v46, v55
	v_mov_b32_e32 v47, v56
	v_mul_f32_e64 v46, v46, s54
	v_mul_f32_e64 v47, v47, s54
	v_fma_mixlo_f16 v1, v54, s54, 0
	s_waitcnt lgkmcnt(0)
	v_pk_mov_b32 v[48:49], v[56:57], v[4:5] op_sel:[1,0]
	v_cvt_pk_f16_f32 v3, v46, v47
	v_pk_mul_f32 v[48:49], v[48:49], s[54:55] op_sel_hi:[1,0]
	v_mov_b32_e32 v4, v5
	v_mov_b32_e32 v5, v6
	v_pack_b32_f16 v46, v1, v3
	v_cvt_pk_f16_f32 v1, v48, v49
	v_pk_mul_f32 v[4:5], v[4:5], s[54:55] op_sel_hi:[1,0]
	v_alignbit_b32 v47, v1, v3, 16
	v_cvt_pk_f16_f32 v3, v4, v5
	ds_read_b128 v[50:53], v2 offset:17472
	v_lshrrev_b32_e32 v49, 16, v3
	v_fma_mixhi_f16 v49, v7, s54, 0
	ds_read_b128 v[4:7], v2 offset:17488
	v_alignbit_b32 v48, v3, v1, 16
	s_waitcnt lgkmcnt(1)
	v_fma_mixlo_f16 v1, v50, s54, 0
	v_mov_b32_e32 v50, v51
	v_mov_b32_e32 v51, v52
	v_pk_mul_f32 v[50:51], v[50:51], s[54:55] op_sel_hi:[1,0]
	s_waitcnt lgkmcnt(0)
	v_pk_mov_b32 v[52:53], v[52:53], v[4:5] op_sel:[1,0]
	v_cvt_pk_f16_f32 v3, v50, v51
	v_pk_mul_f32 v[52:53], v[52:53], s[54:55] op_sel_hi:[1,0]
	v_mov_b32_e32 v4, v5
	v_mov_b32_e32 v5, v6
	v_pack_b32_f16 v50, v1, v3
	v_cvt_pk_f16_f32 v1, v52, v53
	v_pk_mul_f32 v[4:5], v[4:5], s[54:55] op_sel_hi:[1,0]
	v_alignbit_b32 v51, v1, v3, 16
	v_cvt_pk_f16_f32 v3, v4, v5
	ds_read_b128 v[54:57], v0 offset:17536
	v_lshrrev_b32_e32 v53, 16, v3
	v_fma_mixhi_f16 v53, v7, s54, 0
	ds_read_b128 v[4:7], v0 offset:17552
	v_alignbit_b32 v52, v3, v1, 16
	s_waitcnt lgkmcnt(1)
	v_fma_mixlo_f16 v1, v54, s54, 0
	s_mov_b32 s73, 0x3fc00000
	v_mfma_f32_32x32x16_f16 a[0:15], v[46:49], v[50:53], a[0:15]
	v_mov_b32_e32 v46, v55
	v_mov_b32_e32 v47, v56
	v_mul_f32_e64 v46, v46, s54
	v_mul_f32_e64 v47, v47, s54
	s_waitcnt lgkmcnt(0)
	v_pk_mov_b32 v[48:49], v[56:57], v[4:5] op_sel:[1,0]
	v_cvt_pk_f16_f32 v3, v46, v47
	v_pk_mul_f32 v[48:49], v[48:49], s[54:55] op_sel_hi:[1,0]
	v_mov_b32_e32 v4, v5
	v_mov_b32_e32 v5, v6
	v_pack_b32_f16 v46, v1, v3
	v_cvt_pk_f16_f32 v1, v48, v49
	v_pk_mul_f32 v[4:5], v[4:5], s[54:55] op_sel_hi:[1,0]
	v_alignbit_b32 v47, v1, v3, 16
	v_cvt_pk_f16_f32 v3, v4, v5
	ds_read_b128 v[50:53], v2 offset:17536
	v_lshrrev_b32_e32 v49, 16, v3
	v_fma_mixhi_f16 v49, v7, s54, 0
	ds_read_b128 v[4:7], v2 offset:17552
	v_alignbit_b32 v48, v3, v1, 16
	s_waitcnt lgkmcnt(1)
	v_fma_mixlo_f16 v1, v50, s54, 0
	v_mov_b32_e32 v50, v51
	v_mov_b32_e32 v51, v52
	v_pk_mul_f32 v[50:51], v[50:51], s[54:55] op_sel_hi:[1,0]
	s_waitcnt lgkmcnt(0)
	v_pk_mov_b32 v[52:53], v[52:53], v[4:5] op_sel:[1,0]
	v_cvt_pk_f16_f32 v3, v50, v51
	v_pk_mul_f32 v[52:53], v[52:53], s[54:55] op_sel_hi:[1,0]
	v_mov_b32_e32 v4, v5
	v_mov_b32_e32 v5, v6
	v_pack_b32_f16 v50, v1, v3
	v_cvt_pk_f16_f32 v1, v52, v53
	v_pk_mul_f32 v[4:5], v[4:5], s[54:55] op_sel_hi:[1,0]
	v_alignbit_b32 v51, v1, v3, 16
	v_cvt_pk_f16_f32 v3, v4, v5
	ds_read_b128 v[54:57], v0 offset:17600
	v_lshrrev_b32_e32 v53, 16, v3
	v_fma_mixhi_f16 v53, v7, s54, 0
	ds_read_b128 v[4:7], v0 offset:17616
	v_alignbit_b32 v52, v3, v1, 16
	s_waitcnt lgkmcnt(1)
	v_mov_b32_e32 v0, v55
	v_mov_b32_e32 v1, v56
	v_pk_mul_f32 v[0:1], v[0:1], s[54:55] op_sel_hi:[1,0]
	v_fma_mixlo_f16 v3, v54, s54, 0
	v_cvt_pk_f16_f32 v8, v0, v1
	s_waitcnt lgkmcnt(0)
	v_pk_mov_b32 v[0:1], v[56:57], v[4:5] op_sel:[1,0]
	v_mfma_f32_32x32x16_f16 a[0:15], v[46:49], v[50:53], a[0:15]
	v_mul_f32_e64 v0, v0, s54
	v_mul_f32_e64 v1, v1, s54
	v_pack_b32_f16 v46, v3, v8
	v_cvt_pk_f16_f32 v3, v0, v1
	v_mov_b32_e32 v0, v5
	v_mov_b32_e32 v1, v6
	ds_read_b128 v[50:53], v2 offset:17600
	v_pk_mul_f32 v[0:1], v[0:1], s[54:55] op_sel_hi:[1,0]
	v_alignbit_b32 v47, v3, v8, 16
	v_cvt_pk_f16_f32 v0, v0, v1
	v_alignbit_b32 v48, v0, v3, 16
	v_lshrrev_b32_e32 v49, 16, v0
	ds_read_b128 v[0:3], v2 offset:17616
	s_waitcnt lgkmcnt(1)
	v_mov_b32_e32 v4, v51
	v_mov_b32_e32 v5, v52
	v_pk_mul_f32 v[4:5], v[4:5], s[54:55] op_sel_hi:[1,0]
	v_fma_mixlo_f16 v6, v50, s54, 0
	v_cvt_pk_f16_f32 v5, v4, v5
	v_fma_mixhi_f16 v49, v7, s54, 0
	v_pack_b32_f16 v4, v6, v5
	s_waitcnt lgkmcnt(0)
	v_pk_mov_b32 v[6:7], v[52:53], v[0:1] op_sel:[1,0]
	v_mov_b32_e32 v0, v1
	v_mov_b32_e32 v1, v2
	v_pk_mul_f32 v[0:1], v[0:1], s[54:55] op_sel_hi:[1,0]
	v_pk_mul_f32 v[6:7], v[6:7], s[54:55] op_sel_hi:[1,0]
	v_cvt_pk_f16_f32 v0, v0, v1
	v_cvt_pk_f16_f32 v6, v6, v7
	v_lshrrev_b32_e32 v7, 16, v0
	v_alignbit_b32 v5, v6, v5, 16
	v_alignbit_b32 v6, v0, v6, 16
	v_fma_mixhi_f16 v7, v3, s54, 0
	v_add_u32_e32 v8, 0x19800, v60
	ds_read2_b32 v[0:1], v8 offset1:68
	v_mfma_f32_32x32x16_f16 a[0:15], v[46:49], v[4:7], a[0:15]
	s_mov_b32 s54, s52
	s_mov_b32 s55, s52
	s_nop 9
	v_accvgpr_read_b32 v2, a0
	s_waitcnt lgkmcnt(0)
	v_fmamk_f32 v0, v2, 0xb9800000, v0
	ds_read2_b32 v[2:3], v8 offset0:136 offset1:204
	v_accvgpr_read_b32 v4, a1
	v_fmac_f32_e32 v1, 0xb9800000, v4
	ds_write2_b32 v8, v0, v1 offset1:68
	v_accvgpr_read_b32 v0, a2
	v_add_u32_e32 v4, 0x800, v8
	s_waitcnt lgkmcnt(1)
	v_fmamk_f32 v2, v0, 0xb9800000, v2
	ds_read2_b32 v[0:1], v4 offset0:32 offset1:100
	v_accvgpr_read_b32 v5, a3
	v_fmac_f32_e32 v3, 0xb9800000, v5
	ds_write2_b32 v8, v2, v3 offset0:136 offset1:204
	v_accvgpr_read_b32 v2, a4
	s_waitcnt lgkmcnt(1)
	v_fmamk_f32 v0, v2, 0xb9800000, v0
	ds_read2_b32 v[2:3], v4 offset0:168 offset1:236
	v_accvgpr_read_b32 v5, a5
	v_fmac_f32_e32 v1, 0xb9800000, v5
	ds_write2_b32 v4, v0, v1 offset0:32 offset1:100
	v_accvgpr_read_b32 v0, a6
	v_add_u32_e32 v5, 0x1000, v8
	s_waitcnt lgkmcnt(1)
	v_fmamk_f32 v2, v0, 0xb9800000, v2
	ds_read2_b32 v[0:1], v5 offset0:64 offset1:132
	v_accvgpr_read_b32 v6, a7
	v_fmac_f32_e32 v3, 0xb9800000, v6
	ds_write2_b32 v4, v2, v3 offset0:168 offset1:236
	v_accvgpr_read_b32 v2, a8
	v_add_u32_e32 v4, 0x1200, v8
	s_waitcnt lgkmcnt(1)
	v_fmamk_f32 v0, v2, 0xb9800000, v0
	ds_read2_b32 v[2:3], v4 offset0:72 offset1:140
	v_accvgpr_read_b32 v6, a9
	v_fmac_f32_e32 v1, 0xb9800000, v6
	ds_write2_b32 v5, v0, v1 offset0:64 offset1:132
	v_accvgpr_read_b32 v0, a10
	v_add_u32_e32 v5, 0x1800, v8
	s_waitcnt lgkmcnt(1)
	v_fmamk_f32 v2, v0, 0xb9800000, v2
	ds_read2_b32 v[0:1], v5 offset0:96 offset1:164
	v_accvgpr_read_b32 v6, a11
	v_fmac_f32_e32 v3, 0xb9800000, v6
	ds_write2_b32 v4, v2, v3 offset0:72 offset1:140
	v_accvgpr_read_b32 v2, a12
	v_add_u32_e32 v4, 0x1a00, v8
	s_waitcnt lgkmcnt(1)
	v_fmamk_f32 v0, v2, 0xb9800000, v0
	ds_read2_b32 v[2:3], v4 offset0:104 offset1:172
	v_accvgpr_read_b32 v6, a13
	v_fmac_f32_e32 v1, 0xb9800000, v6
	ds_write2_b32 v5, v0, v1 offset0:96 offset1:164
	v_accvgpr_read_b32 v0, a14
	v_accvgpr_read_b32 v1, a15
	s_waitcnt lgkmcnt(1)
	v_fmamk_f32 v0, v0, 0xb9800000, v2
	v_fmac_f32_e32 v3, 0xb9800000, v1
	ds_write2_b32 v4, v0, v3 offset0:104 offset1:172
	v_mov_b64_e32 v[2:3], s[52:53]
	v_add_u32_e32 v0, v12, v34
	v_mov_b64_e32 v[4:5], s[54:55]
	ds_write_b128 v0, v[2:5]
	v_add_u32_e32 v0, v12, v35
	ds_write_b128 v0, v[2:5]
	v_add_u32_e32 v0, v12, v36
	ds_write_b128 v0, v[2:5]
	v_add_u32_e32 v0, v12, v37
	ds_write_b128 v0, v[2:5]
	v_mov_b32_e32 v0, 0x19800
	v_lshl_or_b32 v8, v15, 2, v0
	v_add_u32_e32 v12, 0x1a940, v43
	s_branch .LBB1_330

.LBB1_345:
	s_or_b64 exec, exec, s[52:53]
	s_waitcnt lgkmcnt(2)
	v_rsq_f32_e32 v37, v36
	v_mul_f32_e32 v36, 0.5, v36
	s_lshl_b32 s52, s75, 2
	v_add3_u32 v35, v16, s52, v35
	s_waitcnt lgkmcnt(1)
	v_mul_f32_e32 v43, v36, v37
	v_fma_f32 v43, -v37, v43, s73
	v_mul_f32_e32 v37, v37, v43
	v_mul_f32_e32 v36, v36, v37
	v_fma_f32 v36, -v37, v36, s73
	v_mul_f32_e32 v37, v37, v36
	ds_bpermute_b32 v45, v17, v37
	ds_bpermute_b32 v43, v26, v37
	ds_bpermute_b32 v36, v28, v37
	ds_bpermute_b32 v37, v29, v37
	s_add_i32 s52, s52, 0x19800
	s_waitcnt lgkmcnt(3)
	v_mul_f32_e32 v0, v0, v45
	v_mul_f32_e32 v4, v4, v45
	s_waitcnt lgkmcnt(2)
	v_mul_f32_e32 v5, v5, v43
	v_cndmask_b32_e64 v4, v4, 0, s[38:39]
	v_cndmask_b32_e64 v5, v5, 0, s[40:41]
	ds_write2_b32 v35, v4, v5 offset1:68
	s_waitcnt lgkmcnt(2)
	v_mul_f32_e32 v4, v6, v36
	s_waitcnt lgkmcnt(1)
	v_mul_f32_e32 v5, v7, v37
	v_cndmask_b32_e64 v4, v4, 0, s[42:43]
	v_cndmask_b32_e64 v5, v5, 0, s[48:49]
	v_mul_f32_e32 v1, v1, v43
	v_pk_mul_f32 v[2:3], v[2:3], v[36:37]
	ds_write2_b32 v35, v4, v5 offset0:136 offset1:204
	v_mul_u32_u24_e32 v4, s64, v34
	v_cndmask_b32_e64 v0, v0, 0, s[36:37]
	v_cndmask_b32_e64 v1, 0, v1, s[38:39]
	v_cndmask_b32_e64 v3, v3, 0, s[44:45]
	v_cndmask_b32_e64 v2, v2, 0, s[46:47]
	v_add3_u32 v4, s52, v4, v33
	ds_write_b128 v4, v[0:3]
